# attention unit prologue: the tile-0 mask word is no longer waited for with vmcnt(0) right after its load; its LUT addresses are computed behind the prologue's vmcnt(3)+barrier (on top of v103)
# speedup vs baseline: 1.0088x; 1.0011x over previous
; #define MASK1(p,w,e) ({ unsigned m_; asm("v_bfe_i32 %0, %1, %2, 1":"=v"(m_):"v"(w),"n"(e)); __uint_as_float(__float_as_uint(p)&m_); })
; #define WAIT_BAR(N) asm volatile("s_waitcnt vmcnt(" #N ") lgkmcnt(0)\n\ts_barrier":::"memory")
;   #define DMA_K(t,slot) glds16(ksrc+(long)(t)*KVBLK*DM,(unsigned)__builtin_amdgcn_readfirstlane(kdst+(slot)))
; template<int THRL> __device__ __forceinline__ void attn_unit(int b,int h,int qb,const bf16*Q,const bf16*__restrict__ K,const bf16*__restrict__ V,bf16*O,const unsigned*MASK,char*shm){
;   int tid_=threadIdx.x; asm volatile("":"+v"(tid_));
;   const int tid=tid_,lane=tid&63,r32=lane&31,hi=lane>>5; const int wid=__builtin_amdgcn_readfirstlane(tid>>6);
;   const long rowbase=(long)b*SEQ; const int q0=qb*QB;
;   const bf16*Qw=Q+(rowbase+q0+wid*QBLK)*DM+h*D;
;   const bf16*Kh=K+rowbase*DM+h*D,*Vh=V+rowbase*DM+h*D;
;   const unsigned lds0=(unsigned)(uintptr_t)shm;
;   float*wsf=(float*)(shm+LDS_WS)+wid*64;
;   const bf16*ksrc=Kh+(long)lane*DM+wid*8;
;   const bf16*vsrc=Vh+(long)(16*(wid&3)+(lane>>2))*DM+(wid>>2)*32+(lane&3)*8;
;   const unsigned kdst=lds0+LDS_K+wid*1024, vdst=lds0+LDS_V+wid*1024;
;     ...
;   const int vb0=(int)(lds0+LDS_V)+((lane>>4)&1)*32+(lane&3)*8+(4*hi+((lane&15)>>2))*64;
;   const char*Kbase=shm+LDS_K; bf16x8 kf[8];
;   const lds_cptr shm3=(lds_cptr)shm; const lds_cptr kp0=shm3+LDS_K+hi*1024+r32*16; const lds_cptr vp0=shm3+LDS_V+((lane>>4)&1)*32+(lane&3)*8+(4*hi+((lane&15)>>2))*64;
;   const int NT=(q0+QB)/KVBLK;
;   const unsigned*mwl=MASK+((size_t)(b*256+qb*8+wid)*128)*64+lane;
;   unsigned wA,wB;
;     ...
;   WLOAD(wA,0);WLOAD(wB,1);
;   DMA_K(0,0);DMA_V(0,0);DMA_K(1,SLOTB);
;   bf16x8 qr[4];
;   #pragma unroll
;   for(int d0=0;d0<4;++d0)qr[d0]=*reinterpret_cast<const bf16x8*>(&Qw[(long)r32*DM+d0*16+hi*8]);
;   float mhat=0.f,l_reg=0.f;f32x16 o[2];o[0]=f32x16{};o[1]=f32x16{};f32x16 negm=f32x16{};asm volatile("":"+v"(negm));
;   bool resc=false;
;     ...
;   f32x16 pA0,pA1,pB0,pB1;
;   int sl_prev=0,sl_cur=0,sl_next=SLOTB;
;     ...
;   DMA_K(2,2*SLOTB);
;   WAIT_BAR(3);
;   qkt(pA0,pA1,Kbase,qr,negm,r32,hi);asm volatile("s_nop 15\n\ts_nop 7":"+v"(pA0),"+v"(pA1));
;   START(pA0,pA1);
;   _Pragma("unroll") for(int r=0;r<16;++r)pA1[r]=__builtin_amdgcn_exp2f(pA1[r]);
;   _Pragma("unroll") for(int r=0;r<16;++r){pA0[r]=MASK1(pA0[r],wA,r);pA1[r]=MASK1(pA1[r],wA,16+r);}
;   WAIT_BAR(0);
.LBB0_1271:
	s_ashr_i32 s4, s6, 31
	s_lshr_b32 s4, s4, 29
	s_add_i32 s4, s6, s4
	s_ashr_i32 s42, s4, 3
	v_mov_b32_e32 v58, v0
	s_and_b32 s4, s4, 0x3fffff8
	s_ashr_i32 s43, s42, 31
	v_readfirstlane_b32 s50, v58
	s_lshl_b32 s51, s56, 8
	s_sub_i32 s38, s6, s4
	s_ashr_i32 s7, s50, 6
	s_lshl_b64 s[4:5], s[42:43], 13
	s_ashr_i32 s39, s51, 31
	s_add_u32 s4, s4, s51
	s_addc_u32 s5, s5, s39
	s_lshl_b32 s39, s7, 5
	s_ashr_i32 s40, s39, 31
	s_add_u32 s44, s4, s39
	s_addc_u32 s45, s5, s40
	s_lshl_b64 s[4:5], s[44:45], 10
	s_add_u32 s40, s8, s4
	s_addc_u32 s41, s9, s5
	s_lshl_b32 s4, s38, 6
	s_ashr_i32 s5, s4, 31
	s_lshl_b64 s[38:39], s[4:5], 1
	s_add_u32 s40, s40, s38
	s_addc_u32 s41, s41, s39
	s_lshl_b64 s[4:5], s[42:43], 23
	s_add_u32 s43, s17, s4
	s_addc_u32 s47, s18, s5
	s_add_u32 s46, s43, s38
	s_addc_u32 s47, s47, s39
	s_add_u32 s4, s19, s4
	v_and_b32_e32 v1, 63, v58
	s_addc_u32 s5, s20, s5
	s_add_u32 s48, s4, s38
	v_lshlrev_b32_e32 v2, 10, v1
	s_addc_u32 s49, s5, s39
	v_lshl_add_u64 v[4:5], s[46:47], 0, v[2:3]
	s_lshl_b32 s46, s7, 3
	s_lshl_b32 s4, s7, 4
	v_bfe_u32 v2, v58, 2, 4
	s_ashr_i32 s47, s46, 31
	v_and_or_b32 v2, s4, 48, v2
	s_ashr_i32 s4, s50, 3
	v_lshl_add_u64 v[194:195], s[46:47], 1, v[4:5]
	s_and_b32 s46, s4, 0xffffffe0
	s_and_b32 s5, s50, 0x3fffffc0
	s_ashr_i32 s47, s46, 31
	s_lshl_b32 s58, s7, 10
	s_cmp_lg_u32 0, -1
	s_cselect_b32 s4, 0, 0
	s_lshl_b32 s42, s42, 8
	s_lshl_b32 s43, s56, 3
	s_add_i32 s42, s42, s43
	s_add_i32 s42, s42, s7
	v_lshlrev_b32_e32 v2, 10, v2
	v_lshlrev_b32_e32 v212, 3, v58
	s_add_i32 s58, s58, s4
	s_ashr_i32 s43, s42, 31
	v_lshl_add_u64 v[4:5], s[48:49], 0, v[2:3]
	v_and_b32_e32 v215, 24, v212
	s_add_i32 s59, s58, 0x6000
	s_add_i32 s4, s51, 0x100
	s_lshl_b64 s[42:43], s[42:43], 15
	v_lshl_add_u64 v[4:5], s[46:47], 1, v[4:5]
	v_lshlrev_b32_e32 v2, 1, v215
	s_add_u32 s42, s23, s42
	v_lshl_add_u64 v[208:209], v[4:5], 0, v[2:3]
	s_addc_u32 s43, s54, s43
	v_lshlrev_b32_e32 v2, 2, v1
	v_lshl_add_u64 v[84:85], s[42:43], 0, v[2:3]
	global_load_dword v59, v[84:85], off
	v_lshl_add_u64 v[186:187], v[84:85], 0, s[30:31]
	global_load_dword v218, v[186:187], off
	v_and_b32_e32 v213, 31, v58
	s_mov_b32 s42, m0
	s_mov_b32 m0, s58
	s_nop 0
	global_load_lds_dwordx4 v[194:195], off
	s_mov_b32 m0, s42
	v_bfe_u32 v214, v58, 5, 1
	s_mov_b32 s42, m0
	s_mov_b32 m0, s59
	s_nop 0
	global_load_lds_dwordx4 v[208:209], off
	s_mov_b32 m0, s42
	v_lshlrev_b32_e32 v2, 10, v213
	v_lshl_add_u64 v[4:5], v[194:195], 0, s[36:37]
	s_add_i32 s42, s58, 0x2000
	s_mov_b32 s43, m0
	s_mov_b32 m0, s42
	s_nop 0
	global_load_lds_dwordx4 v[4:5], off
	s_mov_b32 m0, s43
	v_lshl_or_b32 v2, v214, 4, v2
	global_load_dwordx4 v[138:141], v2, s[40:41]
	global_load_dwordx4 v[134:137], v2, s[40:41] offset:32
	global_load_dwordx4 v[126:129], v2, s[40:41] offset:64
	global_load_dwordx4 v[122:125], v2, s[40:41] offset:96
	v_mov_b32_e32 v228, 0
	v_mov_b32_e32 v229, 0
	v_mov_b32_e32 v230, 0
	v_mov_b32_e32 v231, 0
	v_mov_b32_e32 v232, 0
	v_mov_b32_e32 v233, 0
	v_mov_b32_e32 v234, 0
	v_mov_b32_e32 v235, 0
	v_mov_b32_e32 v236, 0
	v_mov_b32_e32 v237, 0
	v_mov_b32_e32 v238, 0
	v_mov_b32_e32 v239, 0
	v_mov_b32_e32 v240, 0
	v_mov_b32_e32 v241, 0
	v_mov_b32_e32 v242, 0
	v_mov_b32_e32 v243, 0
	v_mov_b32_e32 v16, v3
	v_mov_b32_e32 v17, v3
	v_lshlrev_b32_e32 v2, 10, v214
	v_lshlrev_b32_e32 v18, 4, v213
	v_mov_b32_e32 v4, v3
	v_mov_b32_e32 v5, v3
	v_mov_b32_e32 v6, v3
	v_mov_b32_e32 v7, v3
	v_mov_b32_e32 v8, v3
	v_mov_b32_e32 v9, v3
	v_mov_b32_e32 v10, v3
	v_mov_b32_e32 v11, v3
	v_mov_b32_e32 v12, v3
	v_mov_b32_e32 v13, v3
	v_mov_b32_e32 v14, v3
	v_mov_b32_e32 v15, v3
	v_add3_u32 v221, 0, v2, v18
	v_mov_b32_e32 v2, v3
	v_mov_b64_e32 v[32:33], v[16:17]
	v_mov_b64_e32 v[30:31], v[14:15]
	v_mov_b64_e32 v[28:29], v[12:13]
	v_mov_b64_e32 v[26:27], v[10:11]
	v_mov_b64_e32 v[24:25], v[8:9]
	v_mov_b64_e32 v[22:23], v[6:7]
	v_mov_b64_e32 v[20:21], v[4:5]
	v_mov_b64_e32 v[18:19], v[2:3]
	v_lshl_add_u64 v[34:35], v[194:195], 0, s[0:1]
	s_add_i32 s40, s58, 0x4000
	s_mov_b32 s41, m0
	s_mov_b32 m0, s40
	s_nop 0
	global_load_lds_dwordx4 v[34:35], off
	s_mov_b32 m0, s41
	s_waitcnt vmcnt(3) lgkmcnt(0)
	s_barrier
	v_lshlrev_b32_sdwa v225, s32, v59 dst_sel:DWORD dst_unused:UNUSED_PAD src0_sel:DWORD src1_sel:BYTE_0
	v_lshlrev_b32_sdwa v226, s32, v59 dst_sel:DWORD dst_unused:UNUSED_PAD src0_sel:DWORD src1_sel:BYTE_1
	v_lshlrev_b32_sdwa v248, s32, v59 dst_sel:DWORD dst_unused:UNUSED_PAD src0_sel:DWORD src1_sel:BYTE_2
	v_lshlrev_b32_sdwa v249, s32, v59 dst_sel:DWORD dst_unused:UNUSED_PAD src0_sel:DWORD src1_sel:BYTE_3
	ds_read_b128 v[50:53], v221
	ds_read_b128 v[54:57], v221 offset:512
	s_mov_b32 s40, 0xf149f2ca
	s_waitcnt vmcnt(3) lgkmcnt(1)
	v_mfma_f32_32x32x16_bf16 v[34:49], v[50:53], v[138:141], v[18:33]
	v_bfe_i32 v70, v59, 3, 1
	v_bfe_i32 v71, v59, 4, 1
	v_bfe_i32 v72, v59, 5, 1
	v_bfe_i32 v73, v59, 6, 1
	v_bfe_i32 v74, v59, 7, 1
	v_bfe_i32 v75, v59, 8, 1
	v_bfe_i32 v76, v59, 9, 1
	s_waitcnt lgkmcnt(0)
	v_mfma_f32_32x32x16_bf16 v[18:33], v[54:57], v[138:141], v[18:33]
	ds_read_b128 v[50:53], v221 offset:2048
	ds_read_b128 v[54:57], v221 offset:2560
	v_bfe_i32 v77, v59, 10, 1
	v_bfe_i32 v78, v59, 11, 1
	v_bfe_i32 v79, v59, 12, 1
	v_bfe_i32 v80, v59, 13, 1
	v_bfe_i32 v81, v59, 14, 1
	v_bfe_i32 v82, v59, 15, 1
	s_waitcnt vmcnt(2) lgkmcnt(1)
	v_mfma_f32_32x32x16_bf16 v[34:49], v[50:53], v[134:137], v[34:49]
	s_lshl_b32 s5, s5, 2
	v_bfe_i32 v86, v59, 16, 1
	v_bfe_i32 v87, v59, 17, 1
	v_bfe_i32 v69, v59, 2, 1
	s_ashr_i32 s61, s4, 6
	s_add_i32 s57, s5, 0
	v_bfe_i32 v67, v59, 0, 1
	s_waitcnt lgkmcnt(0)
; #define MASK1(p,w,e) ({ unsigned m_; asm("v_bfe_i32 %0, %1, %2, 1":"=v"(m_):"v"(w),"n"(e)); __uint_as_float(__float_as_uint(p)&m_); })
; #define WAIT_BAR(N) asm volatile("s_waitcnt vmcnt(" #N ") lgkmcnt(0)\n\ts_barrier":::"memory")
;   #define DMA_K(t,slot) glds16(ksrc+(long)(t)*KVBLK*DM,(unsigned)__builtin_amdgcn_readfirstlane(kdst+(slot)))
;   #define DMA_V(t,slot) glds16(vsrc+(long)(t)*KVBLK*DM,(unsigned)__builtin_amdgcn_readfirstlane(vdst+(slot)))
;   #define ROT() do{sl_prev=sl_cur;sl_cur=sl_next;sl_next=(sl_next==(NSLOT-1)*SLOTB)?0:sl_next+SLOTB;}while(0)
; template<int THRL> __device__ __forceinline__ void attn_unit(int b,int h,int qb,const bf16*Q,const bf16*__restrict__ K,const bf16*__restrict__ V,bf16*O,const unsigned*MASK,char*shm){
;     ...
;   DMA_K(2,2*SLOTB);
;   WAIT_BAR(3);
;   qkt(pA0,pA1,Kbase,qr,negm,r32,hi);asm volatile("s_nop 15\n\ts_nop 7":"+v"(pA0),"+v"(pA1));
;   START(pA0,pA1);
;   _Pragma("unroll") for(int r=0;r<16;++r)pA1[r]=__builtin_amdgcn_exp2f(pA1[r]);
;   _Pragma("unroll") for(int r=0;r<16;++r){pA0[r]=MASK1(pA0[r],wA,r);pA1[r]=MASK1(pA1[r],wA,16+r);}
;   WAIT_BAR(0);
;   DMA_K(3,0);DMA_V(1,SLOTB);
;   ROT();
;   kload8(kf,kp0+sl_cur);
;   WAIT_BAR(2);
	v_mfma_f32_32x32x16_bf16 v[18:33], v[54:57], v[134:137], v[18:33]
	ds_read_b128 v[50:53], v221 offset:4096
	ds_read_b128 v[54:57], v221 offset:4608
	v_bfe_i32 v68, v59, 1, 1
	s_mov_b32 s92, 1
	s_mov_b32 s48, 0
	s_movk_i32 s60, 0x2000
	s_movk_i32 s62, 0x4000
	v_bfe_i32 v88, v59, 18, 1
	s_waitcnt vmcnt(1) lgkmcnt(1)
	v_mfma_f32_32x32x16_bf16 v[34:49], v[50:53], v[126:129], v[34:49]
	ds_read_b128 v[50:53], v221 offset:6144
	v_bfe_i32 v89, v59, 19, 1
	v_bfe_i32 v90, v59, 20, 1
	v_bfe_i32 v91, v59, 21, 1
	v_bfe_i32 v92, v59, 22, 1
	v_bfe_i32 v93, v59, 23, 1
	v_bfe_i32 v94, v59, 24, 1
	s_waitcnt lgkmcnt(1)
	v_mfma_f32_32x32x16_bf16 v[18:33], v[54:57], v[126:129], v[18:33]
	ds_read_b128 v[54:57], v221 offset:6656
	v_bfe_i32 v95, v59, 25, 1
	v_bfe_i32 v96, v59, 26, 1
	v_bfe_i32 v97, v59, 27, 1
	v_bfe_i32 v98, v59, 28, 1
	v_bfe_i32 v99, v59, 29, 1
	v_bfe_i32 v100, v59, 30, 1
	s_waitcnt vmcnt(0) lgkmcnt(1)
	v_mfma_f32_32x32x16_bf16 v[34:49], v[50:53], v[122:125], v[34:49]
	v_lshlrev_b32_e32 v50, 1, v58
	v_lshlrev_b32_e32 v51, 4, v58
	v_and_b32_e32 v217, 32, v50
	v_and_b32_e32 v50, 0xc0, v51
	v_lshl_or_b32 v216, v214, 8, v50
	v_add_u32_e32 v50, 0, v217
	v_add3_u32 v220, v50, v215, v216
	s_waitcnt lgkmcnt(0)
	v_mfma_f32_32x32x16_bf16 v[18:33], v[54:57], v[122:125], v[18:33]
	s_nop 15
	s_nop 7
	s_nop 0
	v_max3_f32 v50, v34, v35, v18
	v_max3_f32 v51, v36, v37, v19
	s_nop 0
	v_max3_f32 v50, v50, v20, v21
	v_max3_f32 v51, v51, v40, v41
	s_nop 0
	v_max3_f32 v50, v50, v38, v39
	v_max3_f32 v51, v51, v24, v25
	s_nop 0
	v_max3_f32 v50, v50, v22, v23
	v_max3_f32 v51, v51, v44, v45
	s_nop 0
	v_max3_f32 v50, v50, v42, v43
	v_max3_f32 v51, v51, v28, v29
	s_nop 0
	v_max3_f32 v50, v50, v26, v27
	v_max3_f32 v51, v51, v48, v49
	s_nop 0
	v_max3_f32 v50, v50, v46, v47
	v_max3_f32 v51, v51, v32, v33
	s_nop 0
	v_max3_f32 v50, v50, v30, v31
	s_nop 0
	v_max_f32_e32 v50, v50, v51
	s_nop 0
	v_mov_b32_e32 v51, v50
	s_nop 1
	v_permlane32_swap_b32_e32 v50, v51
	v_max_f32_e32 v50, v50, v51
	s_nop 0
	v_cmp_lt_f32_e32 vcc, s40, v50
	v_cmp_gt_u32_e64 s[40:41], 32, v1
	s_nop 0
	v_cndmask_b32_e32 v50, 0, v50, vcc
	v_sub_f32_e32 v18, v18, v50
	v_sub_f32_e32 v19, v19, v50
	v_sub_f32_e32 v52, v36, v50
	v_sub_f32_e32 v53, v37, v50
	v_sub_f32_e32 v54, v38, v50
	v_sub_f32_e32 v55, v39, v50
	v_sub_f32_e32 v56, v40, v50
	v_sub_f32_e32 v57, v41, v50
	v_sub_f32_e32 v58, v42, v50
	v_sub_f32_e32 v60, v43, v50
	v_sub_f32_e32 v61, v44, v50
	v_sub_f32_e32 v62, v45, v50
	v_sub_f32_e32 v63, v46, v50
	v_sub_f32_e32 v64, v47, v50
	v_sub_f32_e32 v65, v48, v50
	v_sub_f32_e32 v66, v49, v50
	s_nop 0
	v_exp_f32_e32 v52, v52
	v_exp_f32_e32 v53, v53
	v_exp_f32_e32 v54, v54
	v_exp_f32_e32 v55, v55
	v_exp_f32_e32 v56, v56
	v_exp_f32_e32 v57, v57
	v_exp_f32_e32 v58, v58
	v_exp_f32_e32 v60, v60
	v_exp_f32_e32 v61, v61
	v_exp_f32_e32 v62, v62
	v_exp_f32_e32 v63, v63
	v_exp_f32_e32 v64, v64
	v_exp_f32_e32 v65, v65
	v_exp_f32_e32 v66, v66
	v_exp_f32_e32 v18, v18
	v_exp_f32_e32 v19, v19
	v_add_f32_e32 v219, v3, v50
	v_sub_f32_e32 v34, v34, v50
	v_sub_f32_e32 v35, v35, v50
	v_sub_f32_e32 v20, v20, v50
	v_sub_f32_e32 v21, v21, v50
	v_sub_f32_e32 v22, v22, v50
	s_nop 0
	v_xor_b32_e32 v36, 0x80000000, v219
	v_sub_f32_e32 v23, v23, v50
	v_sub_f32_e32 v24, v24, v50
	v_sub_f32_e32 v25, v25, v50
	v_sub_f32_e32 v26, v26, v50
	v_sub_f32_e32 v27, v27, v50
	v_sub_f32_e32 v28, v28, v50
	v_sub_f32_e32 v29, v29, v50
	v_sub_f32_e32 v30, v30, v50
	v_sub_f32_e32 v31, v31, v50
	v_sub_f32_e32 v32, v32, v50
	v_sub_f32_e32 v33, v33, v50
	v_mov_b32_e32 v37, v36
	v_mov_b32_e32 v38, v36
	v_mov_b32_e32 v39, v36
	v_mov_b32_e32 v40, v36
	v_mov_b32_e32 v41, v36
	v_mov_b32_e32 v42, v36
	v_mov_b32_e32 v43, v36
	v_mov_b32_e32 v44, v36
	v_mov_b32_e32 v45, v36
	v_mov_b32_e32 v46, v36
	v_mov_b32_e32 v47, v36
	v_mov_b32_e32 v48, v36
	v_mov_b32_e32 v49, v36
	v_mov_b32_e32 v50, v36
	v_mov_b32_e32 v51, v36
	s_waitcnt vmcnt(0) lgkmcnt(0)
	s_barrier
	v_and_b32_e32 v83, v82, v66
	v_and_b32_e32 v82, v81, v65
	v_and_b32_e32 v81, v80, v64
	v_and_b32_e32 v80, v79, v63
	v_and_b32_e32 v79, v78, v62
	v_and_b32_e32 v78, v77, v61
	v_and_b32_e32 v77, v76, v60
	v_and_b32_e32 v76, v75, v58
	v_and_b32_e32 v75, v74, v57
	v_and_b32_e32 v74, v73, v56
	v_and_b32_e32 v73, v72, v55
	v_and_b32_e32 v72, v71, v54
	v_and_b32_e32 v71, v70, v53
	v_and_b32_e32 v70, v69, v52
	v_and_b32_e32 v53, v87, v19
	v_and_b32_e32 v52, v86, v18
	v_lshl_add_u64 v[18:19], v[194:195], 0, s[82:83]
	s_mov_b32 s4, m0
	s_mov_b32 m0, s58
	s_nop 0
	global_load_lds_dwordx4 v[18:19], off
	s_mov_b32 m0, s4
	v_lshl_add_u64 v[18:19], v[208:209], 0, s[36:37]
	s_add_i32 s4, s58, 0x8000
	s_mov_b32 s5, m0
	s_mov_b32 m0, s4
	s_nop 0
	global_load_lds_dwordx4 v[18:19], off
	s_mov_b32 m0, s5
	ds_read_b128 v[178:181], v221 offset:8192
	ds_read_b128 v[170:173], v221 offset:8704
	ds_read_b128 v[174:177], v221 offset:10240
	ds_read_b128 v[162:165], v221 offset:10752
	ds_read_b128 v[166:169], v221 offset:12288
	ds_read_b128 v[154:157], v221 offset:12800
	ds_read_b128 v[158:161], v221 offset:14336
	ds_read_b128 v[150:153], v221 offset:14848
	v_exp_f32_e32 v34, v34
	v_exp_f32_e32 v35, v35
	v_exp_f32_e32 v20, v20
	v_exp_f32_e32 v21, v21
	v_exp_f32_e32 v22, v22
	v_exp_f32_e32 v23, v23
	v_exp_f32_e32 v24, v24
	v_exp_f32_e32 v25, v25
	v_exp_f32_e32 v26, v26
	v_exp_f32_e32 v27, v27
	v_exp_f32_e32 v28, v28
	v_exp_f32_e32 v29, v29
	v_exp_f32_e32 v30, v30
	v_exp_f32_e32 v31, v31
	v_exp_f32_e32 v32, v32
	v_exp_f32_e32 v33, v33
	s_waitcnt vmcnt(2) lgkmcnt(0)
	s_barrier
	v_and_b32_e32 v69, v68, v35
	v_and_b32_e32 v68, v67, v34
	v_bfe_i32 v34, v59, 31, 1
	v_and_b32_e32 v66, v100, v32
	v_and_b32_e32 v67, v34, v33
	v_and_b32_e32 v65, v99, v31
	v_and_b32_e32 v64, v98, v30
	v_and_b32_e32 v63, v97, v29
	v_and_b32_e32 v62, v96, v28
	v_and_b32_e32 v61, v95, v27
	v_and_b32_e32 v60, v94, v26
	v_and_b32_e32 v59, v93, v25
	v_and_b32_e32 v58, v92, v24
	v_and_b32_e32 v57, v91, v23
	v_and_b32_e32 v56, v90, v22
	v_and_b32_e32 v55, v89, v21
	v_and_b32_e32 v54, v88, v20
	s_cmp_lt_i32 s61, 7
	s_cbranch_scc1 .LBB0_1287
	s_mov_b64 s[4:5], 0x50000
	v_lshlrev_b32_e32 v18, 4, v214
	v_lshl_add_u64 v[188:189], v[194:195], 0, s[4:5]
	s_mov_b64 s[4:5], 0x300
	v_mov_b64_e32 v[34:35], v[16:17]
	v_lshl_add_u64 v[192:193], v[84:85], 0, s[4:5]
	v_add_u32_e32 v85, s57, v18
	v_mov_b64_e32 v[32:33], v[14:15]
	v_mov_b64_e32 v[30:31], v[12:13]
	v_mov_b64_e32 v[28:29], v[10:11]
	v_mov_b64_e32 v[26:27], v[8:9]
	v_mov_b64_e32 v[24:25], v[6:7]
	v_mov_b64_e32 v[22:23], v[4:5]
	v_mov_b64_e32 v[20:21], v[2:3]
	v_mov_b64_e32 v[18:19], v[16:17]
	s_add_i32 s46, s61, -5
	v_lshl_add_u32 v210, v213, 2, s57
	v_lshl_add_u64 v[190:191], v[208:209], 0, s[82:83]
	s_mov_b32 s4, 0
	s_movk_i32 s48, 0x4000
	s_movk_i32 s47, 0x2000
	v_mov_b32_e32 v84, 0
	v_mov_b64_e32 v[16:17], v[14:15]
	v_mov_b64_e32 v[14:15], v[12:13]
	v_mov_b64_e32 v[12:13], v[10:11]
	v_mov_b64_e32 v[10:11], v[8:9]
	v_mov_b64_e32 v[8:9], v[6:7]
	v_mov_b64_e32 v[6:7], v[4:5]
	v_mov_b64_e32 v[4:5], v[2:3]
